# v39 + indexer selection: redundant LDS drains between the key-register load batches removed
# baseline (speedup 1.0000x reference)
.LBB0_1297:
	s_and_b64 vcc, exec, s[46:47]
	s_cbranch_vccz .LBB0_1299
	ds_read2st64_b32 v[10:11], v141 offset0:16 offset1:18
	ds_read2st64_b32 v[12:13], v141 offset0:20 offset1:22
	ds_read2st64_b32 v[14:15], v141 offset0:24 offset1:26
	ds_read2st64_b32 v[16:17], v141 offset0:28 offset1:30

.LBB0_1318:
	s_and_b64 vcc, exec, s[48:49]
	s_cbranch_vccz .LBB0_1320
	ds_read2st64_b32 v[82:83], v141 offset0:32 offset1:34
	ds_read2st64_b32 v[84:85], v141 offset0:36 offset1:38
	ds_read2st64_b32 v[86:87], v141 offset0:40 offset1:42
	ds_read2st64_b32 v[88:89], v141 offset0:44 offset1:46

.LBB0_1339:
	s_and_b64 vcc, exec, s[50:51]
	s_cbranch_vccz .LBB0_1341
	ds_read2st64_b32 v[90:91], v141 offset0:48 offset1:50
	ds_read2st64_b32 v[92:93], v141 offset0:52 offset1:54
	ds_read2st64_b32 v[94:95], v141 offset0:56 offset1:58
	ds_read2st64_b32 v[96:97], v141 offset0:60 offset1:62

.LBB0_1360:
	s_and_b64 vcc, exec, s[50:51]
	s_cbranch_vccz .LBB0_1362
	ds_read2st64_b32 v[108:109], v141 offset0:64 offset1:66
	ds_read2st64_b32 v[110:111], v141 offset0:68 offset1:70
	ds_read2st64_b32 v[112:113], v141 offset0:72 offset1:74
	ds_read2st64_b32 v[114:115], v141 offset0:76 offset1:78

.LBB0_1381:
	s_and_b64 vcc, exec, s[50:51]
	s_cbranch_vccz .LBB0_1383
	ds_read2st64_b32 v[116:117], v141 offset0:80 offset1:82
	ds_read2st64_b32 v[118:119], v141 offset0:84 offset1:86
	ds_read2st64_b32 v[120:121], v141 offset0:88 offset1:90
	ds_read2st64_b32 v[122:123], v141 offset0:92 offset1:94

.LBB0_1402:
	s_and_b64 vcc, exec, s[50:51]
	s_cbranch_vccz .LBB0_1404
	ds_read2st64_b32 v[124:125], v141 offset0:96 offset1:98
	ds_read2st64_b32 v[126:127], v141 offset0:100 offset1:102
	ds_read2st64_b32 v[128:129], v141 offset0:104 offset1:106
	ds_read2st64_b32 v[130:131], v141 offset0:108 offset1:110

.LBB0_1423:
	s_and_b64 vcc, exec, s[50:51]
	s_cbranch_vccz .LBB0_1425
	ds_read2st64_b32 v[132:133], v141 offset0:112 offset1:114
	ds_read2st64_b32 v[134:135], v141 offset0:116 offset1:118
	ds_read2st64_b32 v[136:137], v141 offset0:120 offset1:122
	ds_read2st64_b32 v[138:139], v141 offset0:124 offset1:126
